# baseline (speedup 1.0000x reference)
_Z7k_protoPKfPf:
	s_and_b32 s11, s2, 7
	s_lshr_b32 s12, s2, 3
	s_mul_i32 s11, s11, 5
	s_add_i32 s2, s11, s12
	s_load_dwordx4 s[4:7], s[0:1], 0x0
	v_and_b32_e32 v1, 15, v0
	v_lshrrev_b32_e32 v46, 4, v0
	s_lshl_b32 s0, s3, 11
	v_lshl_or_b32 v18, v46, 6, s0
	v_lshlrev_b32_e32 v42, 4, v1
	v_mov_b32_e32 v43, 0
	s_waitcnt lgkmcnt(0)
	v_lshl_add_u64 v[20:21], s[4:5], 0, v[42:43]
	v_ashrrev_i32_e32 v19, 31, v18
	s_mul_i32 s8, s2, 5
	v_lshl_add_u64 v[30:31], v[18:19], 2, v[20:21]
	v_mov_b32_e32 v43, 0x28000
	v_or_b32_e32 v18, 0x400, v18
	v_mad_i64_i32 v[10:11], s[0:1], s8, v43, v[30:31]
	s_add_i32 s4, s8, 1
	s_add_i32 s5, s8, 2
	v_ashrrev_i32_e32 v19, 31, v18
	v_mad_i64_i32 v[12:13], s[0:1], s4, v43, v[30:31]
	global_load_dwordx4 v[2:5], v[10:11], off nt
	global_load_dwordx4 v[6:9], v[12:13], off nt
	v_mad_i64_i32 v[22:23], s[0:1], s5, v43, v[30:31]
	s_add_i32 s9, s8, 3
	v_lshl_add_u64 v[38:39], v[18:19], 2, v[20:21]
	v_mad_i64_i32 v[24:25], s[0:1], s9, v43, v[30:31]
	global_load_dwordx4 v[10:13], v[22:23], off nt
	global_load_dwordx4 v[14:17], v[24:25], off nt
	v_mad_i64_i32 v[18:19], s[0:1], s8, v43, v[38:39]
	v_mad_i64_i32 v[22:23], s[0:1], s4, v43, v[38:39]
	s_add_i32 s10, s8, 4
	global_load_dwordx4 v[18:21], v[18:19], off nt
	v_mad_i64_i32 v[26:27], s[0:1], s5, v43, v[38:39]
	global_load_dwordx4 v[22:25], v[22:23], off nt
	v_mad_i64_i32 v[44:45], s[0:1], s9, v43, v[38:39]
	global_load_dwordx4 v[26:29], v[26:27], off nt
	v_mad_i64_i32 v[40:41], s[0:1], s10, v43, v[30:31]
	global_load_dwordx4 v[30:33], v[44:45], off nt
	global_load_dwordx4 v[34:37], v[40:41], off nt
	v_mad_i64_i32 v[38:39], s[0:1], s10, v43, v[38:39]
	global_load_dwordx4 v[38:41], v[38:39], off nt
	s_movk_i32 s1, 0x120
	s_mov_b32 s0, 0x3e4ccccd
	v_lshrrev_b32_e32 v43, 3, v0
	v_bfe_u32 v44, v0, 4, 2
	v_and_or_b32 v43, v43, 24, v44
	v_lshlrev_b32_e32 v43, 1, v43
	v_mad_u32_u24 v43, v1, s1, v43
	v_cmp_gt_u32_e32 vcc, 64, v0
	s_mul_i32 s4, s2, 20
	v_lshl_or_b32 v42, v46, 8, v42
	s_waitcnt vmcnt(8)
	v_pk_add_f32 v[2:3], v[2:3], v[6:7]
	v_pk_add_f32 v[4:5], v[4:5], v[8:9]
	s_waitcnt vmcnt(7)
	v_pk_add_f32 v[2:3], v[2:3], v[10:11]
	s_waitcnt vmcnt(6)
	v_pk_add_f32 v[2:3], v[2:3], v[14:15]
	v_pk_add_f32 v[4:5], v[4:5], v[12:13]
	s_waitcnt vmcnt(4)
	v_pk_add_f32 v[8:9], v[18:19], v[22:23]
	v_pk_add_f32 v[6:7], v[20:21], v[24:25]
	v_pk_add_f32 v[4:5], v[4:5], v[16:17]
	s_waitcnt vmcnt(3)
	v_pk_add_f32 v[8:9], v[8:9], v[26:27]
	v_pk_add_f32 v[6:7], v[6:7], v[28:29]
	s_waitcnt vmcnt(2)
	v_pk_add_f32 v[8:9], v[8:9], v[30:31]
	s_waitcnt vmcnt(1)
	v_pk_add_f32 v[2:3], v[2:3], v[34:35]
	v_pk_add_f32 v[6:7], v[6:7], v[32:33]
	v_pk_mul_f32 v[2:3], v[2:3], s[0:1] op_sel_hi:[1,0]
	s_waitcnt vmcnt(0)
	v_pk_add_f32 v[8:9], v[8:9], v[38:39]
	v_cvt_f16_f32_e32 v10, v2
	v_pk_add_f32 v[4:5], v[4:5], v[36:37]
	v_pk_add_f32 v[6:7], v[6:7], v[40:41]
	v_pk_mul_f32 v[8:9], v[8:9], s[0:1] op_sel_hi:[1,0]
	v_cvt_f16_f32_e32 v11, v3
	v_pk_mul_f32 v[4:5], v[4:5], s[0:1] op_sel_hi:[1,0]
	v_pk_mul_f32 v[6:7], v[6:7], s[0:1] op_sel_hi:[1,0]
	v_cvt_f16_f32_e32 v12, v8
	v_cvt_f16_f32_e32 v13, v9
	v_pk_mul_f32 v[8:9], v[8:9], v[8:9]
	v_cvt_f16_f32_e32 v14, v4
	v_cvt_f16_f32_e32 v16, v6
	v_cvt_f16_f32_e32 v17, v7
	v_pk_mul_f32 v[6:7], v[6:7], v[6:7]
	v_cvt_f16_f32_e32 v15, v5
	v_pk_fma_f32 v[2:3], v[2:3], v[2:3], v[8:9]
	v_pk_fma_f32 v[4:5], v[4:5], v[4:5], v[6:7]
	ds_write_b16 v43, v10
	ds_write_b16 v43, v11 offset:72
	ds_write_b16 v43, v12 offset:8
	ds_write_b16 v43, v14 offset:144
	ds_write_b16 v43, v15 offset:216
	ds_write_b16 v43, v17 offset:224
	ds_write_b16 v43, v13 offset:80
	ds_write_b16 v43, v16 offset:152
	ds_write_b128 v42, v[2:5] offset:4608
	s_waitcnt lgkmcnt(0)
	s_barrier
	s_mul_hi_i32 s1, s2, 20
	s_ashr_i32 s2, s3, 31
	v_lshrrev_b32_e32 v23, 2, v0
	s_add_u32 s0, s4, s3
	v_and_b32_e32 v23, 48, v23
	s_addc_u32 s1, s1, s2
	v_and_b32_e32 v22, 63, v0
	v_mul_u32_u24_e32 v23, 0x48, v23
	v_mul_u32_u24_e32 v21, 0x48, v1
	v_and_b32_e32 v24, 48, v0
	s_lshl_b64 s[0:1], s[0:1], 8
	v_and_b32_e32 v20, 0xc0, v0
	v_add3_u32 v23, v23, v21, v24
	v_or3_b32 v20, s0, v20, v22
	v_mov_b32_e32 v21, s1
	s_add_u32 s8, s6, 0x32000
	s_addc_u32 s9, s7, 0
	ds_read2_b64 v[26:29], v23 offset1:1
	v_lshl_add_u64 v[24:25], v[20:21], 4, s[8:9]
	s_waitcnt lgkmcnt(0)
	global_store_dwordx4 v[24:25], v[26:29], off
	s_and_saveexec_b64 s[0:1], vcc
	s_cbranch_execz .LBB0_2
	v_lshlrev_b32_e32 v12, 2, v0
	ds_read2st64_b32 v[2:3], v12 offset0:18 offset1:19
	ds_read2st64_b32 v[4:5], v12 offset0:20 offset1:21
	ds_read2st64_b32 v[6:7], v12 offset0:22 offset1:23
	ds_read2st64_b32 v[8:9], v12 offset0:24 offset1:25
	ds_read2st64_b32 v[10:11], v12 offset0:26 offset1:27
	s_waitcnt lgkmcnt(4)
	v_add_f32_e32 v2, 0, v2
	v_add_f32_e32 v2, v2, v3
	s_waitcnt lgkmcnt(3)
	v_add_f32_e32 v2, v2, v4
	v_add_f32_e32 v2, v2, v5
	s_waitcnt lgkmcnt(2)
	v_add_f32_e32 v2, v2, v6
	v_add_f32_e32 v2, v2, v7
	s_waitcnt lgkmcnt(1)
	v_add_f32_e32 v2, v2, v8
	v_add_f32_e32 v8, v2, v9
	ds_read2st64_b32 v[2:3], v12 offset0:28 offset1:29
	ds_read2st64_b32 v[4:5], v12 offset0:30 offset1:31
	ds_read2st64_b32 v[6:7], v12 offset0:32 offset1:33
	s_waitcnt lgkmcnt(3)
	v_add_f32_e32 v8, v8, v10
	v_add_f32_e32 v8, v8, v11
	s_waitcnt lgkmcnt(2)
	v_add_f32_e32 v2, v8, v2
	v_add_f32_e32 v2, v2, v3
	s_waitcnt lgkmcnt(1)
	v_add_f32_e32 v2, v2, v4
	v_add_f32_e32 v2, v2, v5
	s_waitcnt lgkmcnt(0)
	v_add_f32_e32 v2, v2, v6
	s_add_i32 s5, s4, s3
	v_add_f32_e32 v4, v2, v7
	v_lshl_or_b32 v2, s5, 6, v0
	v_ashrrev_i32_e32 v3, 31, v2
	v_lshl_add_u64 v[2:3], v[2:3], 2, s[6:7]
	global_store_dword v[2:3], v4, off
